# fp8 K-loops (G3,G4): LDS-DMA issue without per-piece v_mov / 64-bit VALU address adds (SALU bases), s_not for half masks
# speedup vs baseline: 1.0059x; 1.0059x over previous
.LBB0_1398:
	v_add_u32_e32 v0, s41, v217
	v_add_u32_e32 v12, s44, v217
	ds_read_b128 v[16:19], v0
	ds_read_b128 v[20:23], v0 offset:1024
	ds_read_b128 v[24:27], v0 offset:2048
	ds_read_b128 v[28:31], v0 offset:3072
	ds_read_b128 v[0:3], v12
	ds_read_b128 v[4:7], v12 offset:1024
	ds_read_b128 v[8:11], v12 offset:2048
	ds_read_b128 v[12:15], v12 offset:3072
	s_cmp_eq_u32 s67, 4
	s_cselect_b64 s[0:1], -1, 0
	ds_read_b128 v[56:59], v218
	ds_read_b128 v[60:63], v218 offset:1024
	ds_read_b128 v[48:51], v218 offset:2048
	ds_read_b128 v[52:55], v218 offset:3072
	ds_read_b128 v[40:43], v218 offset:4096
	ds_read_b128 v[44:47], v218 offset:5120
	ds_read_b128 v[32:35], v218 offset:6144
	ds_read_b128 v[36:39], v218 offset:7168
	s_add_i32 m0, s19, 0xc000
	s_and_b64 s[2:3], s[20:21], s[0:1]
	global_load_lds_dwordx4 v214, s[26:27]
	s_add_i32 m0, s19, 0xe000
	s_andn2_b64 vcc, exec, s[2:3]
	global_load_lds_dwordx4 v216, s[26:27]
	s_cbranch_vccnz .LBB0_1400
	s_mov_b32 s2, s86
	v_mbcnt_lo_u32_b32 v64, -1, 0
	v_mbcnt_hi_u32_b32 v64, -1, v64
	s_nop 0
	v_lshl_add_u32 v64, s2, 6, v64
	s_nop 0
	v_ashrrev_i32_e32 v67, 31, v64
	v_lshrrev_b32_e32 v67, 26, v67
	v_lshlrev_b32_e32 v215, 4, v64
	v_lshlrev_b32_e32 v66, 2, v64
	v_add_u32_e32 v67, v64, v67
	v_bfe_i32 v64, v64, 27, 1
	v_lshrrev_b32_e32 v64, 22, v64
	v_add_u32_e32 v64, v215, v64
	v_and_b32_e32 v64, 0xfffffc00, v64
	v_sub_u32_e32 v64, v215, v64
	v_lshrrev_b32_e32 v213, 4, v64
	v_bitop3_b32 v213, v213, v64, 32 bitop3:0x6c
	v_ashrrev_i32_e32 v64, 31, v64
	v_lshrrev_b32_e32 v64, 26, v64
	v_add_u32_e32 v64, v213, v64
	v_and_b32_e32 v66, 0xfc, v66
	v_and_b32_e32 v64, 0xc0, v64
	v_lshrrev_b32_e32 v67, 1, v67
	v_sub_u32_e32 v64, v213, v64
	v_add_u32_e32 v213, s40, v66
	v_and_b32_e32 v214, 32, v67
	ds_read2st64_b32 v[66:67], v213 offset1:1
	ds_read2st64_b32 v[220:221], v213 offset0:2 offset1:3
	v_ashrrev_i16_sdwa v64, v201, sext(v64) dst_sel:DWORD dst_unused:UNUSED_PAD src0_sel:DWORD src1_sel:BYTE_0
	v_bfe_i32 v64, v64, 0, 16
	v_add_lshl_u32 v64, v214, v64, 1
	s_waitcnt lgkmcnt(0)
	v_lshl_add_u32 v213, v66, 10, v64
	v_lshl_add_u32 v214, v220, 10, v64
	v_add_u32_e32 v64, 0x2000, v215
	v_ashrrev_i32_e32 v66, 31, v64
	v_lshrrev_b32_e32 v66, 22, v66
	v_add_u32_e32 v66, v64, v66
	v_ashrrev_i32_e32 v66, 10, v66
	v_mul_i32_i24_e32 v215, 0x400, v66
	v_sub_u32_e32 v64, v64, v215
	v_lshrrev_b32_e32 v215, 4, v64
	v_bitop3_b32 v215, v215, v64, 32 bitop3:0x6c
	v_ashrrev_i32_e32 v64, 31, v64
	v_lshrrev_b32_e32 v64, 26, v64
	v_add_u32_e32 v64, v215, v64
	v_and_b32_e32 v64, 0xc0, v64
	v_sub_u32_e32 v64, v215, v64
	v_lshlrev_b32_e32 v66, 5, v66
	v_ashrrev_i16_sdwa v64, v201, sext(v64) dst_sel:DWORD dst_unused:UNUSED_PAD src0_sel:DWORD src1_sel:BYTE_0
	v_and_b32_e32 v66, 32, v66
	v_bfe_i32 v64, v64, 0, 16
	v_add_lshl_u32 v64, v66, v64, 1
	v_lshl_add_u32 v215, v67, 10, v64
	v_lshl_add_u32 v216, v221, 10, v64
.LBB0_1400:
	s_waitcnt vmcnt(8)
	s_waitcnt lgkmcnt(0)
	s_not_b64 s[2:3], s[24:25]
	s_andn2_b64 vcc, exec, s[24:25]
	s_barrier
	s_cbranch_vccnz .LBB0_1402
	s_setprio 1
	s_waitcnt lgkmcnt(0)
	v_mfma_f32_16x16x128_f8f6f4 v[192:195], v[16:23], v[56:63], v[192:195]
	v_mfma_f32_16x16x128_f8f6f4 v[184:187], v[24:31], v[56:63], v[184:187]
	v_mfma_f32_16x16x128_f8f6f4 v[176:179], v[16:23], v[48:55], v[176:179]
	v_mfma_f32_16x16x128_f8f6f4 v[168:171], v[24:31], v[48:55], v[168:171]
	v_mfma_f32_16x16x128_f8f6f4 v[160:163], v[16:23], v[40:47], v[160:163]
	v_mfma_f32_16x16x128_f8f6f4 v[152:155], v[24:31], v[40:47], v[152:155]
	v_mfma_f32_16x16x128_f8f6f4 v[144:147], v[16:23], v[32:39], v[144:147]
	v_mfma_f32_16x16x128_f8f6f4 v[136:139], v[24:31], v[32:39], v[136:139]
	s_setprio 0
	s_setprio 1
	v_mfma_f32_16x16x128_f8f6f4 v[188:191], v[0:7], v[56:63], v[188:191]
	v_mfma_f32_16x16x128_f8f6f4 v[180:183], v[8:15], v[56:63], v[180:183]
	v_mfma_f32_16x16x128_f8f6f4 v[172:175], v[0:7], v[48:55], v[172:175]
	v_mfma_f32_16x16x128_f8f6f4 v[164:167], v[8:15], v[48:55], v[164:167]
	v_mfma_f32_16x16x128_f8f6f4 v[156:159], v[0:7], v[40:47], v[156:159]
	v_mfma_f32_16x16x128_f8f6f4 v[148:151], v[8:15], v[40:47], v[148:151]
	v_mfma_f32_16x16x128_f8f6f4 v[140:143], v[0:7], v[32:39], v[140:143]
	v_mfma_f32_16x16x128_f8f6f4 v[132:135], v[8:15], v[32:39], v[132:135]
	s_setprio 0
.LBB0_1402:
	s_add_u32 s28, s26, 0x80
	s_addc_u32 s29, s27, 0
	s_and_b64 s[0:1], s[0:1], exec
	v_readlane_b32 s0, v242, 53
	v_readlane_b32 s1, v242, 54
	s_cselect_b32 s29, s1, s29
	s_cselect_b32 s28, s0, s28
	s_cselect_b32 s31, s15, s66
	s_cselect_b32 s30, s64, s65
	s_barrier
	s_mov_b32 m0, s42
	s_waitcnt lgkmcnt(0)
	ds_read_b128 v[56:59], v218 offset:16384
	ds_read_b128 v[60:63], v218 offset:17408
	ds_read_b128 v[48:51], v218 offset:18432
	ds_read_b128 v[52:55], v218 offset:19456
	ds_read_b128 v[40:43], v218 offset:20480
	ds_read_b128 v[44:47], v218 offset:21504
	ds_read_b128 v[32:35], v218 offset:22528
	ds_read_b128 v[36:39], v218 offset:23552
	s_add_u32 s0, s30, 0x20000
	global_load_lds_dwordx4 v211, s[30:31]
	s_mov_b32 m0, s43
	s_addc_u32 s1, s31, 0
	global_load_lds_dwordx4 v212, s[30:31]
	s_mov_b32 m0, s45
	s_andn2_b64 vcc, exec, s[22:23]
	global_load_lds_dwordx4 v211, s[0:1]
	s_mov_b32 m0, s46
	s_nop 0
	global_load_lds_dwordx4 v212, s[0:1]
	s_mov_b32 m0, s19
	s_nop 0
	global_load_lds_dwordx4 v213, s[28:29]
	s_mov_b32 m0, s47
	s_nop 0
	global_load_lds_dwordx4 v215, s[28:29]
	s_waitcnt vmcnt(8)
	s_waitcnt lgkmcnt(0)
	s_not_b64 s[0:1], s[22:23]
	s_barrier
	s_cbranch_vccnz .LBB0_1404
	s_setprio 1
	s_waitcnt lgkmcnt(0)
	v_mfma_f32_16x16x128_f8f6f4 v[128:131], v[16:23], v[56:63], v[128:131]
	v_mfma_f32_16x16x128_f8f6f4 v[120:123], v[24:31], v[56:63], v[120:123]
	v_mfma_f32_16x16x128_f8f6f4 v[112:115], v[16:23], v[48:55], v[112:115]
	v_mfma_f32_16x16x128_f8f6f4 v[104:107], v[24:31], v[48:55], v[104:107]
	v_mfma_f32_16x16x128_f8f6f4 v[96:99], v[16:23], v[40:47], v[96:99]
	v_mfma_f32_16x16x128_f8f6f4 v[88:91], v[24:31], v[40:47], v[88:91]
	v_mfma_f32_16x16x128_f8f6f4 v[80:83], v[16:23], v[32:39], v[80:83]
	v_mfma_f32_16x16x128_f8f6f4 v[72:75], v[24:31], v[32:39], v[72:75]
	s_setprio 0
	s_setprio 1
	v_mfma_f32_16x16x128_f8f6f4 v[124:127], v[0:7], v[56:63], v[124:127]
	v_mfma_f32_16x16x128_f8f6f4 v[116:119], v[8:15], v[56:63], v[116:119]
	v_mfma_f32_16x16x128_f8f6f4 v[108:111], v[0:7], v[48:55], v[108:111]
	v_mfma_f32_16x16x128_f8f6f4 v[100:103], v[8:15], v[48:55], v[100:103]
	v_mfma_f32_16x16x128_f8f6f4 v[92:95], v[0:7], v[40:47], v[92:95]
	v_mfma_f32_16x16x128_f8f6f4 v[84:87], v[8:15], v[40:47], v[84:87]
	v_mfma_f32_16x16x128_f8f6f4 v[76:79], v[0:7], v[32:39], v[76:79]
	v_mfma_f32_16x16x128_f8f6f4 v[68:71], v[8:15], v[32:39], v[68:71]
	s_setprio 0
.LBB0_1404:
	s_barrier
	v_add_u32_e32 v0, s52, v217
	v_add_u32_e32 v12, s57, v217
	ds_read_b128 v[16:19], v0
	ds_read_b128 v[20:23], v0 offset:1024
	ds_read_b128 v[24:27], v0 offset:2048
	ds_read_b128 v[28:31], v0 offset:3072
	ds_read_b128 v[0:3], v12
	ds_read_b128 v[4:7], v12 offset:1024
	ds_read_b128 v[8:11], v12 offset:2048
	ds_read_b128 v[12:15], v12 offset:3072
	s_mov_b32 m0, s48
	ds_read_b128 v[56:59], v218 offset:32768
	ds_read_b128 v[60:63], v218 offset:33792
	ds_read_b128 v[48:51], v218 offset:34816
	ds_read_b128 v[52:55], v218 offset:35840
	ds_read_b128 v[40:43], v218 offset:36864
	ds_read_b128 v[44:47], v218 offset:37888
	ds_read_b128 v[32:35], v218 offset:38912
	ds_read_b128 v[36:39], v218 offset:39936
	s_and_b64 vcc, exec, s[2:3]
	global_load_lds_dwordx4 v214, s[28:29]
	s_mov_b32 m0, s49
	s_nop 0
	global_load_lds_dwordx4 v216, s[28:29]
	s_waitcnt vmcnt(8)
	s_waitcnt lgkmcnt(0)
	s_barrier
	s_cbranch_vccnz .LBB0_1406
	s_setprio 1
	s_waitcnt lgkmcnt(0)
	v_mfma_f32_16x16x128_f8f6f4 v[192:195], v[16:23], v[56:63], v[192:195]
	v_mfma_f32_16x16x128_f8f6f4 v[184:187], v[24:31], v[56:63], v[184:187]
	v_mfma_f32_16x16x128_f8f6f4 v[176:179], v[16:23], v[48:55], v[176:179]
	v_mfma_f32_16x16x128_f8f6f4 v[168:171], v[24:31], v[48:55], v[168:171]
	v_mfma_f32_16x16x128_f8f6f4 v[160:163], v[16:23], v[40:47], v[160:163]
	v_mfma_f32_16x16x128_f8f6f4 v[152:155], v[24:31], v[40:47], v[152:155]
	v_mfma_f32_16x16x128_f8f6f4 v[144:147], v[16:23], v[32:39], v[144:147]
	v_mfma_f32_16x16x128_f8f6f4 v[136:139], v[24:31], v[32:39], v[136:139]
	s_setprio 0
	s_setprio 1
	v_mfma_f32_16x16x128_f8f6f4 v[188:191], v[0:7], v[56:63], v[188:191]
	v_mfma_f32_16x16x128_f8f6f4 v[180:183], v[8:15], v[56:63], v[180:183]
	v_mfma_f32_16x16x128_f8f6f4 v[172:175], v[0:7], v[48:55], v[172:175]
	v_mfma_f32_16x16x128_f8f6f4 v[164:167], v[8:15], v[48:55], v[164:167]
	v_mfma_f32_16x16x128_f8f6f4 v[156:159], v[0:7], v[40:47], v[156:159]
	v_mfma_f32_16x16x128_f8f6f4 v[148:151], v[8:15], v[40:47], v[148:151]
	v_mfma_f32_16x16x128_f8f6f4 v[140:143], v[0:7], v[32:39], v[140:143]
	v_mfma_f32_16x16x128_f8f6f4 v[132:135], v[8:15], v[32:39], v[132:135]
	s_setprio 0
.LBB0_1406:
	s_barrier
	s_waitcnt lgkmcnt(0)
	ds_read_b128 v[56:59], v218 offset:49152
	ds_read_b128 v[60:63], v218 offset:50176
	ds_read_b128 v[48:51], v218 offset:51200
	ds_read_b128 v[52:55], v218 offset:52224
	ds_read_b128 v[40:43], v218 offset:53248
	ds_read_b128 v[44:47], v218 offset:54272
	ds_read_b128 v[32:35], v218 offset:55296
	ds_read_b128 v[36:39], v218 offset:56320
	s_add_u32 s100, s30, s68
	s_addc_u32 s101, s31, s69
	s_mov_b32 m0, s53
	s_add_u32 s2, s30, 0x20080
	global_load_lds_dwordx4 v211, s[100:101]
	s_mov_b32 m0, s54
	s_addc_u32 s3, s31, 0
	global_load_lds_dwordx4 v212, s[100:101]
	s_mov_b32 m0, s58
	s_and_b64 vcc, exec, s[0:1]
	global_load_lds_dwordx4 v211, s[2:3]
	s_mov_b32 m0, s59
	s_add_u32 s100, s28, s68
	global_load_lds_dwordx4 v212, s[2:3]
	s_addc_u32 s101, s29, s69
	s_mov_b32 m0, s55
	s_nop 0
	global_load_lds_dwordx4 v213, s[100:101]
	s_mov_b32 m0, s56
	s_nop 0
	global_load_lds_dwordx4 v215, s[100:101]
	s_waitcnt vmcnt(8)
	s_waitcnt lgkmcnt(0)
	s_barrier
	s_cbranch_vccnz .LBB0_1397
	s_setprio 1
	s_waitcnt lgkmcnt(0)
	v_mfma_f32_16x16x128_f8f6f4 v[128:131], v[16:23], v[56:63], v[128:131]
	v_mfma_f32_16x16x128_f8f6f4 v[120:123], v[24:31], v[56:63], v[120:123]
	v_mfma_f32_16x16x128_f8f6f4 v[112:115], v[16:23], v[48:55], v[112:115]
	v_mfma_f32_16x16x128_f8f6f4 v[104:107], v[24:31], v[48:55], v[104:107]
	v_mfma_f32_16x16x128_f8f6f4 v[96:99], v[16:23], v[40:47], v[96:99]
	v_mfma_f32_16x16x128_f8f6f4 v[88:91], v[24:31], v[40:47], v[88:91]
	v_mfma_f32_16x16x128_f8f6f4 v[80:83], v[16:23], v[32:39], v[80:83]
	v_mfma_f32_16x16x128_f8f6f4 v[72:75], v[24:31], v[32:39], v[72:75]
	s_setprio 0
	s_setprio 1
	v_mfma_f32_16x16x128_f8f6f4 v[124:127], v[0:7], v[56:63], v[124:127]
	v_mfma_f32_16x16x128_f8f6f4 v[116:119], v[8:15], v[56:63], v[116:119]
	v_mfma_f32_16x16x128_f8f6f4 v[108:111], v[0:7], v[48:55], v[108:111]
	v_mfma_f32_16x16x128_f8f6f4 v[100:103], v[8:15], v[48:55], v[100:103]
	v_mfma_f32_16x16x128_f8f6f4 v[92:95], v[0:7], v[40:47], v[92:95]
	v_mfma_f32_16x16x128_f8f6f4 v[84:87], v[8:15], v[40:47], v[84:87]
	v_mfma_f32_16x16x128_f8f6f4 v[76:79], v[0:7], v[32:39], v[76:79]
	v_mfma_f32_16x16x128_f8f6f4 v[68:71], v[8:15], v[32:39], v[68:71]
	s_setprio 0
	s_branch .LBB0_1397

.LBB0_1476:
	v_add_u32_e32 v0, s23, v215
	v_add_u32_e32 v12, s43, v215
	ds_read_b128 v[16:19], v0
	ds_read_b128 v[20:23], v0 offset:1024
	ds_read_b128 v[24:27], v0 offset:2048
	ds_read_b128 v[28:31], v0 offset:3072
	ds_read_b128 v[0:3], v12
	ds_read_b128 v[4:7], v12 offset:1024
	ds_read_b128 v[8:11], v12 offset:2048
	ds_read_b128 v[12:15], v12 offset:3072
	ds_read_b128 v[56:59], v216
	ds_read_b128 v[60:63], v216 offset:1024
	ds_read_b128 v[48:51], v216 offset:2048
	ds_read_b128 v[52:55], v216 offset:3072
	ds_read_b128 v[40:43], v216 offset:4096
	ds_read_b128 v[44:47], v216 offset:5120
	ds_read_b128 v[32:35], v216 offset:6144
	ds_read_b128 v[36:39], v216 offset:7168
	s_add_i32 m0, s46, 0xc000
	s_andn2_b64 vcc, exec, s[28:29]
	global_load_lds_dwordx4 v212, s[30:31]
	s_add_i32 m0, s46, 0xe000
	s_nop 0
	global_load_lds_dwordx4 v214, s[30:31]
	s_waitcnt vmcnt(8)
	s_waitcnt lgkmcnt(0)
	s_not_b64 s[2:3], s[28:29]
	s_barrier
	s_cbranch_vccnz .LBB0_1478
	s_setprio 1
	s_waitcnt lgkmcnt(0)
	v_mfma_f32_16x16x128_f8f6f4 v[192:195], v[16:23], v[56:63], v[192:195]
	v_mfma_f32_16x16x128_f8f6f4 v[188:191], v[24:31], v[56:63], v[188:191]
	v_mfma_f32_16x16x128_f8f6f4 v[176:179], v[16:23], v[48:55], v[176:179]
	v_mfma_f32_16x16x128_f8f6f4 v[172:175], v[24:31], v[48:55], v[172:175]
	v_mfma_f32_16x16x128_f8f6f4 v[160:163], v[16:23], v[40:47], v[160:163]
	v_mfma_f32_16x16x128_f8f6f4 v[156:159], v[24:31], v[40:47], v[156:159]
	v_mfma_f32_16x16x128_f8f6f4 v[144:147], v[16:23], v[32:39], v[144:147]
	v_mfma_f32_16x16x128_f8f6f4 v[140:143], v[24:31], v[32:39], v[140:143]
	s_setprio 0
	s_setprio 1
	v_mfma_f32_16x16x128_f8f6f4 v[184:187], v[0:7], v[56:63], v[184:187]
	v_mfma_f32_16x16x128_f8f6f4 v[180:183], v[8:15], v[56:63], v[180:183]
	v_mfma_f32_16x16x128_f8f6f4 v[168:171], v[0:7], v[48:55], v[168:171]
	v_mfma_f32_16x16x128_f8f6f4 v[164:167], v[8:15], v[48:55], v[164:167]
	v_mfma_f32_16x16x128_f8f6f4 v[152:155], v[0:7], v[40:47], v[152:155]
	v_mfma_f32_16x16x128_f8f6f4 v[148:151], v[8:15], v[40:47], v[148:151]
	v_mfma_f32_16x16x128_f8f6f4 v[136:139], v[0:7], v[32:39], v[136:139]
	v_mfma_f32_16x16x128_f8f6f4 v[132:135], v[8:15], v[32:39], v[132:135]
	s_setprio 0
.LBB0_1478:
	s_add_u32 s0, s30, 0xfffc0080
	s_addc_u32 s1, s31, -1
	s_cmp_eq_u32 s65, 12
	s_cselect_b32 s35, s13, s1
	s_cselect_b32 s34, s62, s0
	s_cselect_b32 s37, s15, s64
	s_cselect_b32 s36, s61, s63
	s_barrier
	s_mov_b32 m0, s25
	s_waitcnt lgkmcnt(0)
	ds_read_b128 v[56:59], v216 offset:16384
	ds_read_b128 v[60:63], v216 offset:17408
	ds_read_b128 v[48:51], v216 offset:18432
	ds_read_b128 v[52:55], v216 offset:19456
	ds_read_b128 v[40:43], v216 offset:20480
	ds_read_b128 v[44:47], v216 offset:21504
	ds_read_b128 v[32:35], v216 offset:22528
	ds_read_b128 v[36:39], v216 offset:23552
	s_add_u32 s0, s36, 0x40000
	global_load_lds_dwordx4 v211, s[36:37]
	s_mov_b32 m0, s42
	s_addc_u32 s1, s37, 0
	global_load_lds_dwordx4 v213, s[36:37]
	s_mov_b32 m0, s44
	s_andn2_b64 vcc, exec, s[26:27]
	global_load_lds_dwordx4 v211, s[0:1]
	s_mov_b32 m0, s45
	s_nop 0
	global_load_lds_dwordx4 v213, s[0:1]
	s_mov_b32 m0, s46
	s_nop 0
	global_load_lds_dwordx4 v212, s[34:35]
	s_mov_b32 m0, s47
	s_nop 0
	global_load_lds_dwordx4 v214, s[34:35]
	s_waitcnt vmcnt(8)
	s_waitcnt lgkmcnt(0)
	s_not_b64 s[0:1], s[26:27]
	s_barrier
	s_cbranch_vccnz .LBB0_1480
	s_setprio 1
	s_waitcnt lgkmcnt(0)
	v_mfma_f32_16x16x128_f8f6f4 v[128:131], v[16:23], v[56:63], v[128:131]
	v_mfma_f32_16x16x128_f8f6f4 v[124:127], v[24:31], v[56:63], v[124:127]
	v_mfma_f32_16x16x128_f8f6f4 v[112:115], v[16:23], v[48:55], v[112:115]
	v_mfma_f32_16x16x128_f8f6f4 v[108:111], v[24:31], v[48:55], v[108:111]
	v_mfma_f32_16x16x128_f8f6f4 v[96:99], v[16:23], v[40:47], v[96:99]
	v_mfma_f32_16x16x128_f8f6f4 v[92:95], v[24:31], v[40:47], v[92:95]
	v_mfma_f32_16x16x128_f8f6f4 v[80:83], v[16:23], v[32:39], v[80:83]
	v_mfma_f32_16x16x128_f8f6f4 v[76:79], v[24:31], v[32:39], v[76:79]
	s_setprio 0
	s_setprio 1
	v_mfma_f32_16x16x128_f8f6f4 v[120:123], v[0:7], v[56:63], v[120:123]
	v_mfma_f32_16x16x128_f8f6f4 v[116:119], v[8:15], v[56:63], v[116:119]
	v_mfma_f32_16x16x128_f8f6f4 v[104:107], v[0:7], v[48:55], v[104:107]
	v_mfma_f32_16x16x128_f8f6f4 v[100:103], v[8:15], v[48:55], v[100:103]
	v_mfma_f32_16x16x128_f8f6f4 v[88:91], v[0:7], v[40:47], v[88:91]
	v_mfma_f32_16x16x128_f8f6f4 v[84:87], v[8:15], v[40:47], v[84:87]
	v_mfma_f32_16x16x128_f8f6f4 v[72:75], v[0:7], v[32:39], v[72:75]
	v_mfma_f32_16x16x128_f8f6f4 v[68:71], v[8:15], v[32:39], v[68:71]
	s_setprio 0
.LBB0_1480:
	s_barrier
	v_add_u32_e32 v0, s52, v215
	v_add_u32_e32 v12, s57, v215
	ds_read_b128 v[16:19], v0
	ds_read_b128 v[20:23], v0 offset:1024
	ds_read_b128 v[24:27], v0 offset:2048
	ds_read_b128 v[28:31], v0 offset:3072
	ds_read_b128 v[0:3], v12
	ds_read_b128 v[4:7], v12 offset:1024
	ds_read_b128 v[8:11], v12 offset:2048
	ds_read_b128 v[12:15], v12 offset:3072
	s_add_u32 s66, s34, 0x40000
	s_mov_b32 m0, s48
	ds_read_b128 v[56:59], v216 offset:32768
	ds_read_b128 v[60:63], v216 offset:33792
	ds_read_b128 v[48:51], v216 offset:34816
	ds_read_b128 v[52:55], v216 offset:35840
	ds_read_b128 v[40:43], v216 offset:36864
	ds_read_b128 v[44:47], v216 offset:37888
	ds_read_b128 v[32:35], v216 offset:38912
	ds_read_b128 v[36:39], v216 offset:39936
	s_addc_u32 s67, s35, 0
	s_and_b64 vcc, exec, s[2:3]
	global_load_lds_dwordx4 v212, s[66:67]
	s_mov_b32 m0, s49
	s_nop 0
	global_load_lds_dwordx4 v214, s[66:67]
	s_waitcnt vmcnt(8)
	s_waitcnt lgkmcnt(0)
	s_barrier
	s_cbranch_vccnz .LBB0_1482
	s_setprio 1
	s_waitcnt lgkmcnt(0)
	v_mfma_f32_16x16x128_f8f6f4 v[192:195], v[16:23], v[56:63], v[192:195]
	v_mfma_f32_16x16x128_f8f6f4 v[188:191], v[24:31], v[56:63], v[188:191]
	v_mfma_f32_16x16x128_f8f6f4 v[176:179], v[16:23], v[48:55], v[176:179]
	v_mfma_f32_16x16x128_f8f6f4 v[172:175], v[24:31], v[48:55], v[172:175]
	v_mfma_f32_16x16x128_f8f6f4 v[160:163], v[16:23], v[40:47], v[160:163]
	v_mfma_f32_16x16x128_f8f6f4 v[156:159], v[24:31], v[40:47], v[156:159]
	v_mfma_f32_16x16x128_f8f6f4 v[144:147], v[16:23], v[32:39], v[144:147]
	v_mfma_f32_16x16x128_f8f6f4 v[140:143], v[24:31], v[32:39], v[140:143]
	s_setprio 0
	s_setprio 1
	v_mfma_f32_16x16x128_f8f6f4 v[184:187], v[0:7], v[56:63], v[184:187]
	v_mfma_f32_16x16x128_f8f6f4 v[180:183], v[8:15], v[56:63], v[180:183]
	v_mfma_f32_16x16x128_f8f6f4 v[168:171], v[0:7], v[48:55], v[168:171]
	v_mfma_f32_16x16x128_f8f6f4 v[164:167], v[8:15], v[48:55], v[164:167]
	v_mfma_f32_16x16x128_f8f6f4 v[152:155], v[0:7], v[40:47], v[152:155]
	v_mfma_f32_16x16x128_f8f6f4 v[148:151], v[8:15], v[40:47], v[148:151]
	v_mfma_f32_16x16x128_f8f6f4 v[136:139], v[0:7], v[32:39], v[136:139]
	v_mfma_f32_16x16x128_f8f6f4 v[132:135], v[8:15], v[32:39], v[132:135]
	s_setprio 0
.LBB0_1482:
	s_barrier
	s_waitcnt lgkmcnt(0)
	ds_read_b128 v[56:59], v216 offset:49152
	ds_read_b128 v[60:63], v216 offset:50176
	ds_read_b128 v[48:51], v216 offset:51200
	ds_read_b128 v[52:55], v216 offset:52224
	ds_read_b128 v[40:43], v216 offset:53248
	ds_read_b128 v[44:47], v216 offset:54272
	ds_read_b128 v[32:35], v216 offset:55296
	ds_read_b128 v[36:39], v216 offset:56320
	s_add_u32 s100, s36, s68
	s_addc_u32 s101, s37, s69
	s_mov_b32 m0, s53
	s_add_u32 s2, s36, 0x40080
	global_load_lds_dwordx4 v211, s[100:101]
	s_mov_b32 m0, s54
	s_addc_u32 s3, s37, 0
	global_load_lds_dwordx4 v213, s[100:101]
	s_mov_b32 m0, s58
	s_and_b64 vcc, exec, s[0:1]
	global_load_lds_dwordx4 v211, s[2:3]
	s_mov_b32 m0, s59
	s_add_u32 s100, s34, s68
	global_load_lds_dwordx4 v213, s[2:3]
	s_addc_u32 s101, s35, s69
	s_mov_b32 m0, s55
	s_nop 0
	global_load_lds_dwordx4 v212, s[100:101]
	s_mov_b32 m0, s56
	s_nop 0
	global_load_lds_dwordx4 v214, s[100:101]
	s_waitcnt vmcnt(8)
	s_waitcnt lgkmcnt(0)
	s_barrier
	s_cbranch_vccnz .LBB0_1475
	s_setprio 1
	s_waitcnt lgkmcnt(0)
	v_mfma_f32_16x16x128_f8f6f4 v[128:131], v[16:23], v[56:63], v[128:131]
	v_mfma_f32_16x16x128_f8f6f4 v[124:127], v[24:31], v[56:63], v[124:127]
	v_mfma_f32_16x16x128_f8f6f4 v[112:115], v[16:23], v[48:55], v[112:115]
	v_mfma_f32_16x16x128_f8f6f4 v[108:111], v[24:31], v[48:55], v[108:111]
	v_mfma_f32_16x16x128_f8f6f4 v[96:99], v[16:23], v[40:47], v[96:99]
	v_mfma_f32_16x16x128_f8f6f4 v[92:95], v[24:31], v[40:47], v[92:95]
	v_mfma_f32_16x16x128_f8f6f4 v[80:83], v[16:23], v[32:39], v[80:83]
	v_mfma_f32_16x16x128_f8f6f4 v[76:79], v[24:31], v[32:39], v[76:79]
	s_setprio 0
	s_setprio 1
	v_mfma_f32_16x16x128_f8f6f4 v[120:123], v[0:7], v[56:63], v[120:123]
	v_mfma_f32_16x16x128_f8f6f4 v[116:119], v[8:15], v[56:63], v[116:119]
	v_mfma_f32_16x16x128_f8f6f4 v[104:107], v[0:7], v[48:55], v[104:107]
	v_mfma_f32_16x16x128_f8f6f4 v[100:103], v[8:15], v[48:55], v[100:103]
	v_mfma_f32_16x16x128_f8f6f4 v[88:91], v[0:7], v[40:47], v[88:91]
	v_mfma_f32_16x16x128_f8f6f4 v[84:87], v[8:15], v[40:47], v[84:87]
	v_mfma_f32_16x16x128_f8f6f4 v[72:75], v[0:7], v[32:39], v[72:75]
	v_mfma_f32_16x16x128_f8f6f4 v[68:71], v[8:15], v[32:39], v[68:71]
	s_setprio 0
	s_branch .LBB0_1475
